# v11 + XCD-local barriers (no L2 write-back, no cross-XCD stage) for the branch->wout and wout->router seams whose producers and consumers share one XCD
# speedup vs baseline: 1.0399x; 1.0049x over previous
.LBB0_1820:
	s_andn2_saveexec_b64 s[6:7], s[6:7]
	s_cbranch_execz .LBB0_1838
	s_mov_b64 s[6:7], exec
	s_waitcnt lgkmcnt(0)
	v_readlane_b32 s6, v254, 19
	v_readlane_b32 s7, v254, 20
	s_waitcnt vmcnt(0)
	s_nop 3
	global_atomic_add v65, v167, s[6:7]
	s_waitcnt vmcnt(0)
